# GEMM phases: static s_setprio raise given to the leading wave half instead of the trailing half (the other half of the v52 experiment)
# speedup vs baseline: 1.0127x; 1.0028x over previous
; #define PG8_BAR __builtin_amdgcn_s_barrier()
;     __host__ __device__ bool next(int i, Unit& u) const {
;         if (i + i0 >= imax) return false; const long L = (long)(i + i0) * G + c; if (L >= nwg) return false;
; template <class Epi, class Sched, bool ALIGN_EPI = false, bool SP2 = false>
; __device__ __forceinline__ void gemm_phase(PG8_LAS unsigned char* lds, const Gemm g, const Sched& S, const Epi& E, const int tid_in) {
;     const int tid = tid_in, wid = __builtin_amdgcn_readfirstlane(tid >> 6), lane = tid & 63, wr = wid >> 2, wc = wid & 3, fr = lane & 15, fq = lane >> 4;
;     const int K = g.K, nt = K / BK, LDB = g.btiled ? 64 : K;
;     unsigned voffA[2], voffB[2]; unsigned vc[2][2] = {{0u, 0u}, {0u, 0u}}, vn[2][2] = {{0u, 0u}, {0u, 0u}}; int gR[2], gC[2];
; #pragma unroll
;     for (int i = 0; i < 2; ++i) { int R, C; stage_rc(tid * 16 + i * 8192, R, C); const int Rb = Epi::PERM ? ((R & ~31) + perm32(R & 31)) : R;
;         voffA[i] = (unsigned)(R * K + C) * 2u; voffB[i] = (unsigned)(Rb * LDB + C) * 2u; gR[i] = R; gC[i] = C * 2; }
;     const size_t kstep = (size_t)(BK * 2);
;     const size_t hstep = (size_t)HALF * K * 2;
;     const size_t tstep = 2 * hstep; const size_t kstepB = g.btiled ? (size_t)32768 : kstep, hstepB = g.btiled ? (size_t)16384 : hstep;
;     const unsigned ldsw = (unsigned)wid * 1024u;
;     const int aoff = lds_byte(wr * 64 + fr, fq * 8), boff = lds_byte(wc * 32 + fr, fq * 8);
;     ...
;     Unit cur, nxt; int ui = 0;
;     if (!S.next(0, cur)) return;
;     f32x4 acc[2][2][4][2];
; #pragma unroll
;     for (int a = 0; a < 2; ++a)
; #pragma unroll
;         for (int b = 0; b < 2; ++b)
; #pragma unroll
;             for (int m = 0; m < 4; ++m)
; #pragma unroll
;                 for (int n = 0; n < 2; ++n) acc[a][b][m][n] = (f32x4){0.f, 0.f, 0.f, 0.f};
;     bf16x8 At[4][2], B0[2][2], B1[2][2];
;     const char* cA = (const char*)g.A + (Sched::GATHER ? (size_t)0 : (size_t)cur.pm * tstep); if constexpr (Sched::GATHER) PG8_GFILL(vc, 0); const char* cB = (const char*)g.Bt + (size_t)cur.pn * tstep + (size_t)cur.e * g.estride;
;     S.a_ready(cur);
;     if constexpr (SP2) {
;         PG8_STAGE(PG8_SB(0, 0), cB, voffB); PG8_STAGE(PG8_SB(0, 1), cB + hstepB, voffB); PG8_STAGE_A(PG8_SA(0, 0), cA, 0, false); PG8_STAGE_A(PG8_SA(0, 1), cA, 1, false);
;         if (wr == 1) PG8_BAR;
.LBB0_191:
	v_ashrrev_i32_e32 v2, 31, v0
	v_lshrrev_b32_e32 v2, 26, v2
	v_lshlrev_b32_e32 v1, 4, v0
	v_add_u32_e32 v2, v0, v2
	v_bfe_i32 v0, v0, 27, 1
	v_lshrrev_b32_e32 v0, 22, v0
	v_add_u32_e32 v0, v1, v0
	v_and_b32_e32 v0, 0xfffffc00, v0
	v_sub_u32_e32 v0, v1, v0
	v_ashrrev_i32_e32 v5, 6, v2
	v_lshrrev_b32_e32 v2, 4, v0
	v_bitop3_b32 v0, v2, v0, 32 bitop3:0x6c
	v_ashrrev_i32_e32 v3, 31, v0
	v_lshrrev_b32_e32 v3, 26, v3
	v_add_u32_e32 v3, v0, v3
	v_lshlrev_b32_e32 v2, 3, v5
	v_ashrrev_i32_e32 v6, 6, v3
	v_and_b32_e32 v3, 0xc0, v3
	v_and_b32_e32 v2, -16, v2
	v_sub_u32_e32 v0, v0, v3
	v_mov_b32_e32 v3, 1
	v_add_u32_e32 v2, v6, v2
	v_lshlrev_b32_e32 v7, 5, v5
	v_ashrrev_i16_sdwa v0, v3, sext(v0) dst_sel:DWORD dst_unused:UNUSED_PAD src0_sel:DWORD src1_sel:BYTE_0
	s_waitcnt vmcnt(19)
	v_and_b32_e32 v8, 32, v7
	v_bfe_i32 v7, v0, 0, 16
	v_lshlrev_b32_e32 v0, 1, v2
	v_lshrrev_b32_e32 v9, 2, v2
	v_and_b32_e32 v10, 3, v6
	s_mov_b32 s3, 0x1ffffe0
	v_and_b32_e32 v0, 24, v0
	v_and_b32_e32 v9, 4, v9
	v_and_or_b32 v10, v2, s3, v10
	v_or3_b32 v0, v10, v9, v0
	v_add_lshl_u32 v8, v8, v7, 1
	v_lshl_add_u32 v138, v0, 7, v8
	v_add_u32_e32 v0, 0x2000, v1
	v_ashrrev_i32_e32 v1, 31, v0
	v_lshrrev_b32_e32 v1, 22, v1
	v_add_u32_e32 v1, v0, v1
	v_lshl_add_u32 v136, v2, 12, v8
	v_ashrrev_i32_e32 v8, 10, v1
	v_mul_i32_i24_e32 v1, 0x400, v8
	v_sub_u32_e32 v0, v0, v1
	s_load_dwordx2 s[30:31], s[6:7], 0xc8
	v_lshrrev_b32_e32 v1, 4, v0
	v_bitop3_b32 v0, v1, v0, 32 bitop3:0x6c
	v_ashrrev_i32_e32 v2, 31, v0
	v_lshrrev_b32_e32 v2, 26, v2
	v_add_u32_e32 v2, v0, v2
	s_waitcnt lgkmcnt(0)
	s_add_u32 s22, s30, 0x36000000
	v_lshlrev_b32_e32 v1, 3, v8
	v_ashrrev_i32_e32 v9, 6, v2
	v_and_b32_e32 v2, 0xc0, v2
	s_addc_u32 s23, s31, 0
	v_and_b32_e32 v1, -16, v1
	v_sub_u32_e32 v0, v0, v2
	s_add_u32 s24, s30, 0x800000
	v_add_u32_e32 v1, v9, v1
	v_ashrrev_i16_sdwa v0, v3, sext(v0) dst_sel:DWORD dst_unused:UNUSED_PAD src0_sel:DWORD src1_sel:BYTE_0
	v_and_b32_e32 v3, 3, v9
	s_addc_u32 s25, s31, 0
	s_ashr_i32 s5, s4, 6
	v_and_or_b32 v3, v1, s3, v3
	s_ashr_i32 s3, s2, 31
	s_ashr_i32 s51, s50, 31
	s_ashr_i32 s6, s4, 8
	s_lshl_b32 s58, s5, 10
	s_lshl_b64 s[8:9], s[2:3], 20
	s_lshl_b64 s[10:11], s[50:51], 20
	v_lshlrev_b32_e32 v10, 5, v8
	s_add_u32 s52, s24, s10
	v_and_b32_e32 v11, 32, v10
	v_bfe_i32 v10, v0, 0, 16
	v_lshlrev_b32_e32 v0, 1, v1
	v_lshrrev_b32_e32 v2, 2, v1
	s_addc_u32 s53, s25, s11
	s_add_i32 s59, s58, 0
	v_and_b32_e32 v0, 24, v0
	v_and_b32_e32 v2, 4, v2
	s_add_i32 m0, s59, 0x10000
	v_or3_b32 v0, v3, v2, v0
	v_add_lshl_u32 v2, v11, v10, 1
	global_load_lds_dwordx4 v138, s[52:53]
	s_add_i32 m0, s59, 0x12000
	v_lshl_add_u32 v142, v0, 7, v2
	s_add_u32 s10, s52, 0x4000
	global_load_lds_dwordx4 v142, s[52:53]
	s_addc_u32 s11, s53, 0
	s_add_i32 m0, s59, 0x14000
	v_lshl_add_u32 v140, v1, 12, v2
	global_load_lds_dwordx4 v138, s[10:11]
	s_add_i32 m0, s59, 0x16000
	s_add_u32 s54, s22, s8
	s_addc_u32 s55, s23, s9
	s_add_i32 s60, s59, 0x2000
	global_load_lds_dwordx4 v142, s[10:11]
	s_mov_b32 m0, s59
	s_add_u32 s8, s54, 0x80000
	global_load_lds_dwordx4 v136, s[54:55]
	s_mov_b32 m0, s60
	s_addc_u32 s9, s55, 0
	s_add_i32 s61, s59, 0x4000
	global_load_lds_dwordx4 v140, s[54:55]
	s_mov_b32 m0, s61
	s_add_i32 s62, s59, 0x6000
	global_load_lds_dwordx4 v136, s[8:9]
	s_mov_b32 m0, s62
	v_mov_b32_e32 v145, 0
	global_load_lds_dwordx4 v140, s[8:9]
	v_mov_b32_e32 v137, v145
	v_mov_b32_e32 v141, v145
	s_cmp_eq_u32 s6, 1
	s_mov_b32 s7, 0
	v_mov_b32_e32 v139, v145
	v_mov_b32_e32 v143, v145
	v_lshl_add_u64 v[0:1], s[54:55], 0, v[136:137]
	s_cselect_b64 s[8:9], -1, 0
	s_cmp_lg_u32 s6, 1
	v_lshl_add_u64 v[2:3], s[54:55], 0, v[140:141]
	s_setprio 1
	s_cbranch_scc1 .LBB0_193
	s_setprio 0
	s_barrier

; #define PG8_BAR __builtin_amdgcn_s_barrier()
;     __host__ __device__ bool next(int i, Unit& u) const {
;         if (i + i0 >= imax) return false; const long L = (long)(i + i0) * G + c; if (L >= nwg) return false;
; template <class Epi, class Sched, bool ALIGN_EPI = false, bool SP2 = false>
; __device__ __forceinline__ void gemm_phase(PG8_LAS unsigned char* lds, const Gemm g, const Sched& S, const Epi& E, const int tid_in) {
;     const int tid = tid_in, wid = __builtin_amdgcn_readfirstlane(tid >> 6), lane = tid & 63, wr = wid >> 2, wc = wid & 3, fr = lane & 15, fq = lane >> 4;
;     const int K = g.K, nt = K / BK, LDB = g.btiled ? 64 : K;
;     unsigned voffA[2], voffB[2]; unsigned vc[2][2] = {{0u, 0u}, {0u, 0u}}, vn[2][2] = {{0u, 0u}, {0u, 0u}}; int gR[2], gC[2];
; #pragma unroll
;     for (int i = 0; i < 2; ++i) { int R, C; stage_rc(tid * 16 + i * 8192, R, C); const int Rb = Epi::PERM ? ((R & ~31) + perm32(R & 31)) : R;
;         voffA[i] = (unsigned)(R * K + C) * 2u; voffB[i] = (unsigned)(Rb * LDB + C) * 2u; gR[i] = R; gC[i] = C * 2; }
;     const size_t kstep = (size_t)(BK * 2);
;     const size_t hstep = (size_t)HALF * K * 2;
;     const size_t tstep = 2 * hstep; const size_t kstepB = g.btiled ? (size_t)32768 : kstep, hstepB = g.btiled ? (size_t)16384 : hstep;
;     const unsigned ldsw = (unsigned)wid * 1024u;
;     const int aoff = lds_byte(wr * 64 + fr, fq * 8), boff = lds_byte(wc * 32 + fr, fq * 8);
;     ...
;     Unit cur, nxt; int ui = 0;
;     if (!S.next(0, cur)) return;
;     f32x4 acc[2][2][4][2];
; #pragma unroll
;     for (int a = 0; a < 2; ++a)
; #pragma unroll
;         for (int b = 0; b < 2; ++b)
; #pragma unroll
;             for (int m = 0; m < 4; ++m)
; #pragma unroll
;                 for (int n = 0; n < 2; ++n) acc[a][b][m][n] = (f32x4){0.f, 0.f, 0.f, 0.f};
;     bf16x8 At[4][2], B0[2][2], B1[2][2];
;     const char* cA = (const char*)g.A + (Sched::GATHER ? (size_t)0 : (size_t)cur.pm * tstep); if constexpr (Sched::GATHER) PG8_GFILL(vc, 0); const char* cB = (const char*)g.Bt + (size_t)cur.pn * tstep + (size_t)cur.e * g.estride;
;     S.a_ready(cur);
;     if constexpr (SP2) {
;         PG8_STAGE(PG8_SB(0, 0), cB, voffB); PG8_STAGE(PG8_SB(0, 1), cB + hstepB, voffB); PG8_STAGE_A(PG8_SA(0, 0), cA, 0, false); PG8_STAGE_A(PG8_SA(0, 1), cA, 1, false);
;         if (wr == 1) PG8_BAR;
.LBB0_767:
	s_cmp_lt_i32 s84, 6
	s_cselect_b64 s[2:3], -1, 0
	s_cmp_gt_i32 s85, 5
	s_cselect_b64 s[4:5], -1, 0
	s_and_b64 s[2:3], s[2:3], s[4:5]
	s_andn2_b64 vcc, exec, s[2:3]
	s_cbranch_vccnz .LBB0_845
	s_mov_b64 s[2:3], s[0:1]
	s_waitcnt vmcnt(0)
	v_mbcnt_lo_u32_b32 v1, -1, 0
	v_mbcnt_hi_u32_b32 v1, -1, v1
	s_cmpk_gt_i32 s81, 0xff
	v_add_u32_e32 v0, s33, v1
	s_nop 0
	v_readfirstlane_b32 s4, v0
	s_cbranch_scc1 .LBB0_795
	v_lshlrev_b32_e32 v2, 4, v0
	v_add_u32_e32 v3, 0x2000, v2
	s_waitcnt lgkmcnt(0)
	v_ashrrev_i32_e32 v4, 31, v3
	v_lshrrev_b32_e32 v4, 22, v4
	v_add_u32_e32 v4, v3, v4
	v_ashrrev_i32_e32 v6, 10, v4
	v_mul_i32_i24_e32 v4, 0x400, v6
	v_sub_u32_e32 v3, v3, v4
	v_lshrrev_b32_e32 v4, 4, v3
	v_bitop3_b32 v3, v4, v3, 32 bitop3:0x6c
	v_ashrrev_i32_e32 v4, 31, v3
	v_lshrrev_b32_e32 v4, 26, v4
	v_add_u32_e32 v4, v3, v4
	v_lshlrev_b32_e32 v5, 3, v6
	v_ashrrev_i32_e32 v7, 6, v4
	v_and_b32_e32 v5, -16, v5
	v_add_u32_e32 v5, v7, v5
	s_load_dwordx2 s[12:13], s[2:3], 0xc8
	v_and_b32_e32 v8, 3, v7
	s_mov_b32 s2, 0x1ffffe0
	v_lshrrev_b32_e32 v9, 2, v5
	v_lshlrev_b32_e32 v10, 1, v5
	v_and_b32_e32 v4, 0xc0, v4
	v_and_or_b32 v8, v5, s2, v8
	v_and_b32_e32 v9, 4, v9
	v_and_b32_e32 v10, 24, v10
	v_sub_u32_e32 v3, v3, v4
	v_mov_b32_e32 v4, 1
	v_or3_b32 v9, v8, v9, v10
	v_lshlrev_b32_e32 v8, 5, v6
	v_ashrrev_i16_sdwa v3, v4, sext(v3) dst_sel:DWORD dst_unused:UNUSED_PAD src0_sel:DWORD src1_sel:BYTE_0
	v_and_b32_e32 v10, 32, v8
	v_bfe_i32 v8, v3, 0, 16
	v_add_lshl_u32 v3, v10, v8, 1
	v_lshl_add_u32 v132, v9, 7, v3
	v_lshl_add_u32 v134, v5, 13, v3
	v_bfe_i32 v3, v0, 27, 1
	v_lshrrev_b32_e32 v3, 22, v3
	v_add_u32_e32 v3, v2, v3
	v_and_b32_e32 v3, 0xfffffc00, v3
	v_sub_u32_e32 v2, v2, v3
	v_lshrrev_b32_e32 v3, 4, v2
	v_ashrrev_i32_e32 v5, 31, v0
	v_bitop3_b32 v2, v3, v2, 32 bitop3:0x6c
	v_lshrrev_b32_e32 v5, 26, v5
	v_ashrrev_i32_e32 v3, 31, v2
	v_add_u32_e32 v0, v0, v5
	s_waitcnt lgkmcnt(0)
	s_add_u32 s17, s12, 0x4c000000
	v_lshrrev_b32_e32 v3, 26, v3
	v_ashrrev_i32_e32 v10, 6, v0
	s_addc_u32 s54, s13, 0
	v_add_u32_e32 v3, v2, v3
	v_lshlrev_b32_e32 v0, 3, v10
	s_add_u32 s55, s12, 0x4800000
	v_ashrrev_i32_e32 v9, 6, v3
	v_and_b32_e32 v0, -16, v0
	s_addc_u32 s56, s13, 0
	v_add_u32_e32 v0, v9, v0
	v_and_b32_e32 v5, 3, v9
	s_ashr_i32 s58, s81, 31
	v_and_or_b32 v5, v0, s2, v5
	s_lshr_b32 s2, s58, 29
	s_add_i32 s2, s81, s2
	s_and_b32 s3, s2, -8
	s_ashr_i32 s14, s4, 6
	s_sub_i32 s3, s81, s3
	s_ashr_i32 s5, s4, 8
	s_lshl_b32 s57, s14, 10
	s_lshl_b32 s7, s3, 5
	s_ashr_i32 s2, s2, 3
	s_mul_i32 s6, s3, 33
	s_cmp_lt_i32 s3, 0
	s_cselect_b32 s3, s6, s7
	s_add_i32 s2, s3, s2
	s_ashr_i32 s3, s2, 31
	s_lshr_b32 s3, s3, 26
	s_add_i32 s3, s2, s3
	v_lshrrev_b32_e32 v11, 2, v0
	v_lshlrev_b32_e32 v12, 1, v0
	v_and_b32_e32 v3, 0xc0, v3
	s_ashr_i32 s6, s3, 6
	v_and_b32_e32 v11, 4, v11
	v_and_b32_e32 v12, 24, v12
	v_sub_u32_e32 v2, v2, v3
	s_lshl_b32 s6, s6, 3
	v_or3_b32 v5, v5, v11, v12
	v_lshlrev_b32_e32 v11, 5, v10
	v_ashrrev_i16_sdwa v2, v4, sext(v2) dst_sel:DWORD dst_unused:UNUSED_PAD src0_sel:DWORD src1_sel:BYTE_0
	s_sub_i32 s7, 32, s6
	v_and_b32_e32 v12, 32, v11
	v_bfe_i32 v11, v2, 0, 16
	s_min_u32 s7, s7, 8
	s_andn2_b32 s3, s3, 63
	v_add_lshl_u32 v2, v12, v11, 1
	s_sub_i32 s8, s2, s3
	v_cvt_f32_ubyte0_e32 v4, s7
	v_lshl_add_u32 v136, v5, 7, v2
	v_cvt_f32_i32_e32 v3, s8
	v_rcp_iflag_f32_e32 v5, v4
	v_lshl_add_u32 v138, v0, 13, v2
	s_ashr_i32 s2, s8, 30
	s_or_b32 s9, s2, 1
	v_mul_f32_e32 v0, v3, v5
	v_trunc_f32_e32 v0, v0
	v_fma_f32 v2, -v0, v4, v3
	v_cvt_i32_f32_e32 v0, v0
	v_cmp_ge_f32_e64 s[2:3], |v2|, v4
	s_and_b64 s[2:3], s[2:3], exec
	s_cselect_b32 s2, s9, 0
	v_readfirstlane_b32 s3, v0
	s_add_i32 s26, s3, s2
	s_mul_i32 s2, s26, s7
	s_sub_i32 s2, s8, s2
	s_sext_i32_i8 s2, s2
	s_add_i32 s2, s6, s2
	s_ashr_i32 s3, s2, 31
	s_bfe_i64 s[8:9], s[26:27], 0x80000
	s_lshl_b64 s[6:7], s[2:3], 21
	s_lshl_b64 s[8:9], s[8:9], 21
	s_add_u32 s42, s55, s8
	s_addc_u32 s43, s56, s9
	s_add_i32 s59, s57, 0
	s_add_i32 m0, s59, 0x10000
	v_mov_b32_e32 v0, 0
	global_load_lds_dwordx4 v136, s[42:43]
	s_add_i32 m0, s59, 0x12000
	s_add_u32 s8, s42, 0x4000
	global_load_lds_dwordx4 v132, s[42:43]
	s_addc_u32 s9, s43, 0
	s_add_i32 m0, s59, 0x14000
	v_mov_b32_e32 v139, v0
	global_load_lds_dwordx4 v136, s[8:9]
	s_add_i32 m0, s59, 0x16000
	s_add_u32 s44, s17, s6
	s_addc_u32 s45, s54, s7
	s_add_i32 s60, s59, 0x2000
	global_load_lds_dwordx4 v132, s[8:9]
	s_mov_b32 m0, s59
	s_add_u32 s6, s44, 0x100000
	global_load_lds_dwordx4 v138, s[44:45]
	s_mov_b32 m0, s60
	s_addc_u32 s7, s45, 0
	s_add_i32 s61, s59, 0x4000
	global_load_lds_dwordx4 v134, s[44:45]
	s_mov_b32 m0, s61
	s_add_i32 s62, s59, 0x6000
	global_load_lds_dwordx4 v138, s[6:7]
	s_mov_b32 m0, s62
	v_mov_b32_e32 v135, v0
	global_load_lds_dwordx4 v134, s[6:7]
	s_cmp_eq_u32 s5, 1
	s_mov_b32 s3, 0
	v_mov_b32_e32 v137, v0
	v_mov_b32_e32 v133, v0
	s_mov_b64 s[6:7], 0x4000
	v_lshl_add_u64 v[4:5], s[44:45], 0, v[138:139]
	v_lshl_add_u64 v[2:3], s[44:45], 0, v[134:135]
	s_cselect_b64 s[8:9], -1, 0
	s_cmp_lg_u32 s5, 1
	s_movk_i32 s63, 0x4000
	s_setprio 1
	s_cbranch_scc1 .LBB0_771
	s_setprio 0
	s_barrier

; #define PG8_BAR __builtin_amdgcn_s_barrier()
;     __host__ __device__ bool next(int i, Unit& u) const {
;         if (i + i0 >= imax) return false; const long L = (long)(i + i0) * G + c; if (L >= nwg) return false;
; template <class Epi, class Sched, bool ALIGN_EPI = false, bool SP2 = false>
; __device__ __forceinline__ void gemm_phase(PG8_LAS unsigned char* lds, const Gemm g, const Sched& S, const Epi& E, const int tid_in) {
;     const int tid = tid_in, wid = __builtin_amdgcn_readfirstlane(tid >> 6), lane = tid & 63, wr = wid >> 2, wc = wid & 3, fr = lane & 15, fq = lane >> 4;
;     const int K = g.K, nt = K / BK, LDB = g.btiled ? 64 : K;
;     unsigned voffA[2], voffB[2]; unsigned vc[2][2] = {{0u, 0u}, {0u, 0u}}, vn[2][2] = {{0u, 0u}, {0u, 0u}}; int gR[2], gC[2];
; #pragma unroll
;     for (int i = 0; i < 2; ++i) { int R, C; stage_rc(tid * 16 + i * 8192, R, C); const int Rb = Epi::PERM ? ((R & ~31) + perm32(R & 31)) : R;
;         voffA[i] = (unsigned)(R * K + C) * 2u; voffB[i] = (unsigned)(Rb * LDB + C) * 2u; gR[i] = R; gC[i] = C * 2; }
;     const size_t kstep = (size_t)(BK * 2);
;     const size_t hstep = (size_t)HALF * K * 2;
;     const size_t tstep = 2 * hstep; const size_t kstepB = g.btiled ? (size_t)32768 : kstep, hstepB = g.btiled ? (size_t)16384 : hstep;
;     const unsigned ldsw = (unsigned)wid * 1024u;
;     const int aoff = lds_byte(wr * 64 + fr, fq * 8), boff = lds_byte(wc * 32 + fr, fq * 8);
;     ...
;     Unit cur, nxt; int ui = 0;
;     if (!S.next(0, cur)) return;
;     f32x4 acc[2][2][4][2];
; #pragma unroll
;     for (int a = 0; a < 2; ++a)
; #pragma unroll
;         for (int b = 0; b < 2; ++b)
; #pragma unroll
;             for (int m = 0; m < 4; ++m)
; #pragma unroll
;                 for (int n = 0; n < 2; ++n) acc[a][b][m][n] = (f32x4){0.f, 0.f, 0.f, 0.f};
;     bf16x8 At[4][2], B0[2][2], B1[2][2];
;     const char* cA = (const char*)g.A + (Sched::GATHER ? (size_t)0 : (size_t)cur.pm * tstep); if constexpr (Sched::GATHER) PG8_GFILL(vc, 0); const char* cB = (const char*)g.Bt + (size_t)cur.pn * tstep + (size_t)cur.e * g.estride;
;     S.a_ready(cur);
;     if constexpr (SP2) {
;         PG8_STAGE(PG8_SB(0, 0), cB, voffB); PG8_STAGE(PG8_SB(0, 1), cB + hstepB, voffB); PG8_STAGE_A(PG8_SA(0, 0), cA, 0, false); PG8_STAGE_A(PG8_SA(0, 1), cA, 1, false);
;         if (wr == 1) PG8_BAR;
.LBB0_845:
	s_cmp_lt_i32 s84, 8
	s_cselect_b64 s[2:3], -1, 0
	s_cmp_gt_i32 s85, 7
	s_cselect_b64 s[4:5], -1, 0
	s_and_b64 s[2:3], s[2:3], s[4:5]
	s_andn2_b64 vcc, exec, s[2:3]
	s_cbranch_vccnz .LBB0_917
	s_mov_b64 s[6:7], s[0:1]
	s_waitcnt vmcnt(0) lgkmcnt(0)
	v_mbcnt_lo_u32_b32 v4, -1, 0
	v_mbcnt_hi_u32_b32 v4, -1, v4
	s_cmpk_gt_i32 s81, 0xff
	v_add_u32_e32 v0, s33, v4
	s_nop 0
	v_readfirstlane_b32 s4, v0
	s_cbranch_scc1 .LBB0_867
	v_lshlrev_b32_e32 v1, 4, v0
	v_add_u32_e32 v2, 0x2000, v1
	v_ashrrev_i32_e32 v3, 31, v2
	v_lshrrev_b32_e32 v3, 22, v3
	v_add_u32_e32 v3, v2, v3
	v_ashrrev_i32_e32 v5, 10, v3
	v_mul_i32_i24_e32 v6, 0x400, v5
	v_sub_u32_e32 v2, v2, v6
	v_lshrrev_b32_e32 v6, 4, v2
	v_bitop3_b32 v2, v6, v2, 32 bitop3:0x6c
	v_ashrrev_i32_e32 v6, 31, v2
	v_lshrrev_b32_e32 v6, 26, v6
	v_add_u32_e32 v7, v2, v6
	v_ashrrev_i32_e32 v6, 6, v7
	v_and_b32_e32 v7, 0xc0, v7
	v_sub_u32_e32 v2, v2, v7
	v_mov_b32_e32 v10, 1
	s_load_dwordx2 s[10:11], s[6:7], 0xc8
	s_load_dwordx2 s[2:3], s[6:7], 0x0
	v_lshlrev_b32_e32 v3, 5, v5
	v_ashrrev_i16_sdwa v2, v10, sext(v2) dst_sel:DWORD dst_unused:UNUSED_PAD src0_sel:DWORD src1_sel:BYTE_0
	v_and_b32_e32 v3, 32, v3
	v_bfe_i32 v7, v2, 0, 16
	v_add_u32_e32 v2, v3, v7
	v_lshlrev_b32_e32 v3, 3, v5
	v_and_b32_e32 v3, -16, v3
	s_waitcnt lgkmcnt(0)
	s_add_u32 s17, s10, 0x54000000
	v_add_u32_e32 v3, v6, v3
	s_addc_u32 s22, s11, 0
	v_lshlrev_b32_e32 v8, 7, v3
	s_add_u32 s23, s10, 0x5800000
	v_lshl_add_u32 v144, v2, 1, v8
	s_movk_i32 s8, 0xf80
	v_ashrrev_i32_e32 v2, 31, v0
	s_addc_u32 s24, s11, 0
	v_mad_u64_u32 v[146:147], s[6:7], v3, s8, v[144:145]
	v_lshrrev_b32_e32 v2, 26, v2
	s_ashr_i32 s54, s81, 31
	v_add_u32_e32 v2, v0, v2
	v_bfe_i32 v0, v0, 27, 1
	s_lshr_b32 s6, s54, 29
	v_lshrrev_b32_e32 v0, 22, v0
	s_add_i32 s6, s81, s6
	v_add_u32_e32 v0, v1, v0
	s_and_b32 s7, s6, -8
	s_ashr_i32 s5, s4, 6
	v_and_b32_e32 v0, 0xfffffc00, v0
	s_sub_i32 s7, s81, s7
	s_ashr_i32 s15, s4, 8
	s_lshl_b32 s25, s5, 10
	v_sub_u32_e32 v0, v1, v0
	s_lshl_b32 s12, s7, 5
	s_ashr_i32 s6, s6, 3
	v_lshrrev_b32_e32 v1, 4, v0
	s_mul_i32 s9, s7, 33
	s_cmp_lt_i32 s7, 0
	v_bitop3_b32 v0, v1, v0, 32 bitop3:0x6c
	s_cselect_b32 s7, s9, s12
	v_ashrrev_i32_e32 v1, 31, v0
	s_add_i32 s6, s7, s6
	v_lshrrev_b32_e32 v1, 26, v1
	s_ashr_i32 s7, s6, 31
	v_add_u32_e32 v1, v0, v1
	s_lshr_b32 s7, s7, 26
	v_ashrrev_i32_e32 v8, 6, v2
	v_ashrrev_i32_e32 v9, 6, v1
	v_and_b32_e32 v1, 0xc0, v1
	s_add_i32 s7, s6, s7
	v_sub_u32_e32 v0, v0, v1
	v_lshlrev_b32_e32 v1, 3, v8
	s_ashr_i32 s9, s7, 6
	v_lshlrev_b32_e32 v2, 5, v8
	v_ashrrev_i16_sdwa v0, v10, sext(v0) dst_sel:DWORD dst_unused:UNUSED_PAD src0_sel:DWORD src1_sel:BYTE_0
	v_and_b32_e32 v1, -16, v1
	s_lshl_b32 s9, s9, 3
	v_and_b32_e32 v2, 32, v2
	v_bfe_i32 v10, v0, 0, 16
	v_add_u32_e32 v1, v9, v1
	s_sub_i32 s12, 32, s9
	v_add_u32_e32 v0, v2, v10
	v_lshlrev_b32_e32 v2, 7, v1
	s_min_u32 s12, s12, 8
	s_andn2_b32 s7, s7, 63
	v_lshl_add_u32 v148, v0, 1, v2
	s_sub_i32 s13, s6, s7
	v_cvt_f32_ubyte0_e32 v2, s12
	v_cvt_f32_i32_e32 v0, s13
	v_rcp_iflag_f32_e32 v3, v2
	v_mad_u64_u32 v[150:151], s[6:7], v1, s8, v[148:149]
	s_ashr_i32 s6, s13, 30
	v_mul_f32_e32 v1, v0, v3
	v_trunc_f32_e32 v1, v1
	v_fma_f32 v0, -v1, v2, v0
	v_cvt_i32_f32_e32 v1, v1
	s_or_b32 s8, s6, 1
	v_cmp_ge_f32_e64 s[6:7], |v0|, v2
	s_and_b64 s[6:7], s[6:7], exec
	s_cselect_b32 s6, s8, 0
	v_readfirstlane_b32 s7, v1
	s_add_i32 s14, s7, s6
	s_mul_i32 s6, s14, s12
	s_sub_i32 s6, s13, s6
	s_sext_i32_i8 s6, s6
	s_add_i32 s46, s9, s6
	s_ashr_i32 s47, s46, 31
	s_bfe_i64 s[8:9], s[14:15], 0x80000
	s_lshl_b64 s[6:7], s[46:47], 20
	s_lshl_b64 s[8:9], s[8:9], 20
	s_add_u32 s48, s23, s8
	s_addc_u32 s49, s24, s9
	s_add_i32 s47, s25, 0
	s_add_i32 m0, s47, 0x10000
	v_mov_b32_e32 v149, 0
	global_load_lds_dwordx4 v148, s[48:49]
	s_add_i32 m0, s47, 0x12000
	s_add_u32 s8, s48, 0x4000
	global_load_lds_dwordx4 v144, s[48:49]
	s_addc_u32 s9, s49, 0
	s_add_i32 m0, s47, 0x14000
	v_mov_b32_e32 v151, v149
	global_load_lds_dwordx4 v148, s[8:9]
	s_add_i32 m0, s47, 0x16000
	s_add_u32 s50, s17, s6
	s_addc_u32 s51, s22, s7
	s_add_i32 s18, s47, 0x2000
	global_load_lds_dwordx4 v144, s[8:9]
	s_mov_b32 m0, s47
	s_add_u32 s6, s50, 0x80000
	global_load_lds_dwordx4 v150, s[50:51]
	s_mov_b32 m0, s18
	s_addc_u32 s7, s51, 0
	s_add_i32 s19, s47, 0x4000
	global_load_lds_dwordx4 v146, s[50:51]
	s_mov_b32 m0, s19
	s_add_i32 s55, s47, 0x6000
	global_load_lds_dwordx4 v150, s[6:7]
	s_mov_b32 m0, s55
	v_mov_b32_e32 v147, v149
	global_load_lds_dwordx4 v146, s[6:7]
	s_cmp_eq_u32 s15, 1
	s_mov_b32 s56, 0
	v_mov_b32_e32 v145, v149
	v_lshl_add_u64 v[0:1], s[50:51], 0, v[150:151]
	s_cselect_b64 s[6:7], -1, 0
	s_cmp_lg_u32 s15, 1
	v_lshl_add_u64 v[2:3], s[50:51], 0, v[146:147]
	s_setprio 1
	s_cbranch_scc1 .LBB0_849
	s_setprio 0
	s_barrier

; #define PG8_BAR __builtin_amdgcn_s_barrier()
;     __device__ __forceinline__ bool next(int i, Unit& u) const {
;         if (i + i0 >= imax) return false; const long L = (long)(i + i0) * G + c; if (L >= nwg) return false;
; template <class Epi, class Sched, bool ALIGN_EPI = false, bool SP2 = false>
; __device__ __forceinline__ void gemm_phase(PG8_LAS unsigned char* lds, const Gemm g, const Sched& S, const Epi& E, const int tid_in) {
;     const int tid = tid_in, wid = __builtin_amdgcn_readfirstlane(tid >> 6), lane = tid & 63, wr = wid >> 2, wc = wid & 3, fr = lane & 15, fq = lane >> 4;
;     const int K = g.K, nt = K / BK, LDB = g.btiled ? 64 : K;
;     unsigned voffA[2], voffB[2]; unsigned vc[2][2] = {{0u, 0u}, {0u, 0u}}, vn[2][2] = {{0u, 0u}, {0u, 0u}}; int gR[2], gC[2];
; #pragma unroll
;     for (int i = 0; i < 2; ++i) { int R, C; stage_rc(tid * 16 + i * 8192, R, C); const int Rb = Epi::PERM ? ((R & ~31) + perm32(R & 31)) : R;
;         voffA[i] = (unsigned)(R * K + C) * 2u; voffB[i] = (unsigned)(Rb * LDB + C) * 2u; gR[i] = R; gC[i] = C * 2; }
;     const size_t kstep = (size_t)(BK * 2);
;     const size_t hstep = (size_t)HALF * K * 2;
;     const size_t tstep = 2 * hstep; const size_t kstepB = g.btiled ? (size_t)32768 : kstep, hstepB = g.btiled ? (size_t)16384 : hstep;
;     const unsigned ldsw = (unsigned)wid * 1024u;
;     const int aoff = lds_byte(wr * 64 + fr, fq * 8), boff = lds_byte(wc * 32 + fr, fq * 8);
;     ...
;     Unit cur, nxt; int ui = 0;
;     if (!S.next(0, cur)) return;
;     f32x4 acc[2][2][4][2];
; #pragma unroll
;     for (int a = 0; a < 2; ++a)
; #pragma unroll
;         for (int b = 0; b < 2; ++b)
; #pragma unroll
;             for (int m = 0; m < 4; ++m)
; #pragma unroll
;                 for (int n = 0; n < 2; ++n) acc[a][b][m][n] = (f32x4){0.f, 0.f, 0.f, 0.f};
;     bf16x8 At[4][2], B0[2][2], B1[2][2];
;     const char* cA = (const char*)g.A + (Sched::GATHER ? (size_t)0 : (size_t)cur.pm * tstep); if constexpr (Sched::GATHER) PG8_GFILL(vc, 0); const char* cB = (const char*)g.Bt + (size_t)cur.pn * tstep + (size_t)cur.e * g.estride;
;     S.a_ready(cur);
;     if constexpr (SP2) {
;         PG8_STAGE(PG8_SB(0, 0), cB, voffB); PG8_STAGE(PG8_SB(0, 1), cB + hstepB, voffB); PG8_STAGE_A(PG8_SA(0, 0), cA, 0, false); PG8_STAGE_A(PG8_SA(0, 1), cA, 1, false);
;         if (wr == 1) PG8_BAR;
.LBB0_2190:
	s_add_u32 s14, s8, 0x36000000
	s_addc_u32 s15, s9, 0
	s_add_u32 s64, s8, 0x6000000
	s_addc_u32 s65, s9, 0
	s_ashr_i32 s2, s81, 3
	s_mul_i32 s2, s2, 9
	s_waitcnt lgkmcnt(0)
	s_barrier
	s_load_dwordx2 s[12:13], s[12:13], 0xa0
	s_ashr_i32 s68, s2, 5
	s_add_u32 s26, s8, 0x64000000
	s_addc_u32 s27, s9, 0
	s_cmp_lt_i32 s68, 1
	s_cbranch_scc1 .LBB0_2210
	v_mbcnt_lo_u32_b32 v2, -1, 0
	v_mbcnt_hi_u32_b32 v2, -1, v2
	s_andn2_b64 vcc, exec, s[28:29]
	v_add_u32_e32 v0, s33, v2
	s_nop 0
	v_readfirstlane_b32 s2, v0
	s_cbranch_vccnz .LBB0_2210
	v_ashrrev_i32_e32 v3, 31, v0
	v_lshrrev_b32_e32 v3, 26, v3
	v_lshlrev_b32_e32 v1, 4, v0
	v_add_u32_e32 v3, v0, v3
	v_bfe_i32 v0, v0, 27, 1
	v_lshrrev_b32_e32 v0, 22, v0
	v_add_u32_e32 v0, v1, v0
	v_and_b32_e32 v0, 0xfffffc00, v0
	v_sub_u32_e32 v0, v1, v0
	v_lshrrev_b32_e32 v4, 4, v0
	v_bitop3_b32 v0, v4, v0, 32 bitop3:0x6c
	v_ashrrev_i32_e32 v5, 31, v0
	v_ashrrev_i32_e32 v3, 6, v3
	v_lshrrev_b32_e32 v5, 26, v5
	v_lshlrev_b32_e32 v4, 3, v3
	v_add_u32_e32 v5, v0, v5
	v_and_b32_e32 v4, -16, v4
	v_ashrrev_i32_e32 v6, 6, v5
	v_add_u32_e32 v160, v6, v4
	v_and_b32_e32 v4, 0xc0, v5
	v_sub_u32_e32 v0, v0, v4
	v_mov_b32_e32 v4, 1
	v_lshlrev_b32_e32 v3, 5, v3
	v_ashrrev_i16_sdwa v0, v4, sext(v0) dst_sel:DWORD dst_unused:UNUSED_PAD src0_sel:DWORD src1_sel:BYTE_0
	v_and_b32_e32 v3, 32, v3
	v_bfe_i32 v0, v0, 0, 16
	v_add_lshl_u32 v161, v3, v0, 1
	v_add_u32_e32 v0, 0x2000, v1
	v_ashrrev_i32_e32 v1, 31, v0
	v_lshrrev_b32_e32 v1, 22, v1
	v_add_u32_e32 v1, v0, v1
	v_ashrrev_i32_e32 v1, 10, v1
	v_mul_i32_i24_e32 v3, 0x400, v1
	v_sub_u32_e32 v0, v0, v3
	v_lshrrev_b32_e32 v3, 4, v0
	v_bitop3_b32 v0, v3, v0, 32 bitop3:0x6c
	s_ashr_i32 s4, s2, 6
	s_ashr_i32 s3, s2, 8
	v_ashrrev_i32_e32 v5, 31, v0
	s_lshl_b32 s22, s4, 10
	s_or_b32 s23, s63, 1
	v_lshrrev_b32_e32 v5, 26, v5
	s_cmp_lt_i32 s5, 0
	v_lshlrev_b32_e32 v3, 3, v1
	v_add_u32_e32 v5, v0, v5
	s_cselect_b32 s20, s23, s63
	v_and_b32_e32 v3, -16, v3
	v_ashrrev_i32_e32 v7, 6, v5
	s_mul_i32 s5, s20, s5
	v_add_u32_e32 v162, v7, v3
	v_and_b32_e32 v3, 0xc0, v5
	s_add_i32 s20, s5, s18
	v_sub_u32_e32 v0, v0, v3
	s_ashr_i32 s5, s20, 31
	v_lshlrev_b32_e32 v1, 5, v1
	v_ashrrev_i16_sdwa v0, v4, sext(v0) dst_sel:DWORD dst_unused:UNUSED_PAD src0_sel:DWORD src1_sel:BYTE_0
	s_lshr_b32 s5, s5, 28
	v_and_b32_e32 v1, 32, v1
	v_bfe_i32 v0, v0, 0, 16
	s_add_i32 s5, s20, s5
	v_add_lshl_u32 v163, v1, v0, 1
	v_and_b32_e32 v0, 3, v7
	s_mov_b32 s19, 0x1ffffe0
	v_lshrrev_b32_e32 v1, 2, v162
	v_lshlrev_b32_e32 v3, 1, v162
	s_ashr_i32 s5, s5, 4
	v_and_or_b32 v0, v162, s19, v0
	v_and_b32_e32 v1, 4, v1
	v_and_b32_e32 v3, 24, v3
	s_lshl_b32 s5, s5, 2
	s_add_i32 s24, 0, 0x26c00
	v_or3_b32 v0, v0, v1, v3
	s_add_i32 s5, s24, s5
	v_lshl_add_u32 v144, v0, 7, v163
	v_mov_b32_e32 v0, s5
	ds_read_b32 v88, v0
	v_and_b32_e32 v0, 3, v6
	v_and_or_b32 v3, v160, s19, v0
	v_lshrrev_b32_e32 v0, 2, v160
	v_and_b32_e32 v4, 4, v0
	s_waitcnt lgkmcnt(0)
	v_lshlrev_b32_e32 v0, 2, v88
	v_add_u32_e32 v0, s24, v0
	ds_read2st64_b32 v[0:1], v0 offset0:4 offset1:5
	v_lshlrev_b32_e32 v5, 1, v160
	v_and_b32_e32 v5, 24, v5
	v_or3_b32 v3, v3, v4, v5
	v_lshl_add_u32 v146, v3, 7, v161
	s_waitcnt lgkmcnt(0)
	v_readfirstlane_b32 s5, v1
	s_addk_i32 s5, 0xff
	s_ashr_i32 s5, s5, 8
	s_abs_i32 s21, s5
	v_cvt_f32_u32_e32 v1, s21
	v_readfirstlane_b32 s18, v0
	s_ashr_i32 s18, s18, 8
	s_sub_i32 s28, 0, s21
	v_rcp_iflag_f32_e32 v0, v1
	s_lshl_b32 s19, s18, 4
	s_sub_i32 s19, s20, s19
	s_abs_i32 s25, s19
	v_mul_f32_e32 v0, 0x4f7ffffe, v0
	v_cvt_u32_f32_e32 v0, v0
	s_xor_b32 s20, s19, s5
	s_ashr_i32 s20, s20, 31
	v_lshlrev_b32_e32 v3, 2, v162
	v_readfirstlane_b32 s29, v0
	s_mul_i32 s28, s28, s29
	s_mul_hi_u32 s28, s29, s28
	s_add_i32 s29, s29, s28
	s_mul_hi_u32 s28, s25, s29
	s_mul_i32 s29, s28, s21
	s_sub_i32 s25, s25, s29
	s_add_i32 s29, s28, 1
	s_sub_i32 s30, s25, s21
	s_cmp_ge_u32 s25, s21
	s_cselect_b32 s28, s29, s28
	s_cselect_b32 s25, s30, s25
	s_add_i32 s29, s28, 1
	s_cmp_ge_u32 s25, s21
	s_cselect_b32 s21, s29, s28
	v_lshlrev_b32_e32 v0, 2, v160
	s_add_i32 s25, 0, 0x20000
	v_add_u32_e32 v1, s25, v0
	v_add_u32_e32 v4, s25, v3
	s_add_i32 s25, 0, 0x20200
	s_xor_b32 s21, s21, s20
	v_add_u32_e32 v0, s25, v0
	v_add_u32_e32 v3, s25, v3
	ds_read_b32 v1, v1
	ds_read_b32 v4, v4
	ds_read_b32 v0, v0
	ds_read_b32 v3, v3
	s_sub_i32 s56, s21, s20
	s_ashr_i32 s57, s56, 31
	s_lshl_b64 s[20:21], s[56:57], 20
	v_ashrrev_i32_e32 v89, 31, v88
	s_add_u32 s20, s64, s20
	s_waitcnt lgkmcnt(3)
	v_lshl_add_u32 v148, v1, 12, v161
	s_waitcnt lgkmcnt(1)
	v_lshl_add_u32 v92, v0, 12, v161
	s_addc_u32 s21, s65, s21
	v_lshlrev_b64 v[0:1], 24, v[88:89]
	v_lshl_add_u64 v[0:1], s[20:21], 0, v[0:1]
	s_add_i32 s25, s22, 0
	s_add_i32 m0, s25, 0x10000
	v_readfirstlane_b32 s20, v0
	v_readfirstlane_b32 s21, v1
	s_mov_b64 s[28:29], 0x4000
	v_lshl_add_u32 v94, v4, 12, v163
	v_lshl_add_u64 v[4:5], v[0:1], 0, s[28:29]
	s_add_i32 s57, s25, 0x2000
	s_add_i32 s67, s25, 0x4000
	global_load_lds_dwordx4 v146, s[20:21]
	s_add_i32 m0, s25, 0x12000
	s_add_i32 s69, s25, 0x6000
	global_load_lds_dwordx4 v144, s[20:21]
	s_add_i32 m0, s25, 0x14000
	v_readfirstlane_b32 s20, v4
	v_readfirstlane_b32 s21, v5
	s_waitcnt lgkmcnt(0)
	v_lshl_add_u32 v90, v3, 12, v163
	v_mov_b32_e32 v149, 0
	s_mov_b32 s70, 0
	v_mov_b32_e32 v147, v149
	v_mov_b32_e32 v145, v149
	global_load_lds_dwordx4 v146, s[20:21]
	s_add_i32 m0, s25, 0x16000
	s_cmp_eq_u32 s3, 1
	global_load_lds_dwordx4 v144, s[20:21]
	s_mov_b32 m0, s25
	s_cselect_b64 s[30:31], -1, 0
	global_load_lds_dwordx4 v148, s[14:15]
	s_mov_b32 m0, s57
	s_cmp_lg_u32 s3, 1
	global_load_lds_dwordx4 v94, s[14:15]
	s_mov_b32 m0, s67
	v_mov_b32_e32 v95, v149
	global_load_lds_dwordx4 v92, s[14:15]
	s_mov_b32 m0, s69
	s_nop 0
	global_load_lds_dwordx4 v90, s[14:15]
	s_setprio 1
	s_cbranch_scc1 .LBB0_2194
	s_setprio 0
	s_barrier

; #define PG8_BAR __builtin_amdgcn_s_barrier()
;     __device__ __forceinline__ bool next(int i, Unit& u) const {
;         if (i + i0 >= imax) return false; const long L = (long)(i + i0) * G + c; if (L >= nwg) return false;
; template <class Epi, class Sched, bool ALIGN_EPI = false, bool SP2 = false>
; __device__ __forceinline__ void gemm_phase(PG8_LAS unsigned char* lds, const Gemm g, const Sched& S, const Epi& E, const int tid_in) {
;     const int tid = tid_in, wid = __builtin_amdgcn_readfirstlane(tid >> 6), lane = tid & 63, wr = wid >> 2, wc = wid & 3, fr = lane & 15, fq = lane >> 4;
;     const int K = g.K, nt = K / BK, LDB = g.btiled ? 64 : K;
;     unsigned voffA[2], voffB[2]; unsigned vc[2][2] = {{0u, 0u}, {0u, 0u}}, vn[2][2] = {{0u, 0u}, {0u, 0u}}; int gR[2], gC[2];
; #pragma unroll
;     for (int i = 0; i < 2; ++i) { int R, C; stage_rc(tid * 16 + i * 8192, R, C); const int Rb = Epi::PERM ? ((R & ~31) + perm32(R & 31)) : R;
;         voffA[i] = (unsigned)(R * K + C) * 2u; voffB[i] = (unsigned)(Rb * LDB + C) * 2u; gR[i] = R; gC[i] = C * 2; }
;     const size_t kstep = (size_t)(BK * 2);
;     const size_t hstep = (size_t)HALF * K * 2;
;     const size_t tstep = 2 * hstep; const size_t kstepB = g.btiled ? (size_t)32768 : kstep, hstepB = g.btiled ? (size_t)16384 : hstep;
;     const unsigned ldsw = (unsigned)wid * 1024u;
;     const int aoff = lds_byte(wr * 64 + fr, fq * 8), boff = lds_byte(wc * 32 + fr, fq * 8);
;     ...
;     Unit cur, nxt; int ui = 0;
;     if (!S.next(0, cur)) return;
;     f32x4 acc[2][2][4][2];
; #pragma unroll
;     for (int a = 0; a < 2; ++a)
; #pragma unroll
;         for (int b = 0; b < 2; ++b)
; #pragma unroll
;             for (int m = 0; m < 4; ++m)
; #pragma unroll
;                 for (int n = 0; n < 2; ++n) acc[a][b][m][n] = (f32x4){0.f, 0.f, 0.f, 0.f};
;     bf16x8 At[4][2], B0[2][2], B1[2][2];
;     const char* cA = (const char*)g.A + (Sched::GATHER ? (size_t)0 : (size_t)cur.pm * tstep); if constexpr (Sched::GATHER) PG8_GFILL(vc, 0); const char* cB = (const char*)g.Bt + (size_t)cur.pn * tstep + (size_t)cur.e * g.estride;
;     S.a_ready(cur);
;     if constexpr (SP2) {
;         PG8_STAGE(PG8_SB(0, 0), cB, voffB); PG8_STAGE(PG8_SB(0, 1), cB + hstepB, voffB); PG8_STAGE_A(PG8_SA(0, 0), cA, 0, false); PG8_STAGE_A(PG8_SA(0, 1), cA, 1, false);
;         if (wr == 1) PG8_BAR;
.LBB0_2288:
	s_mul_i32 s2, s16, s68
	s_mul_hi_i32 s3, s16, s68
	s_add_u32 s2, s2, s81
	s_addc_u32 s3, s3, s62
	s_waitcnt vmcnt(21)
	v_mov_b64_e32 v[4:5], s[10:11]
	s_waitcnt lgkmcnt(0)
	s_barrier
	v_mbcnt_lo_u32_b32 v2, -1, 0
	v_mbcnt_hi_u32_b32 v2, -1, v2
	v_cmp_ge_i64_e32 vcc, s[2:3], v[4:5]
	v_add_u32_e32 v0, s33, v2
	s_nop 0
	v_readfirstlane_b32 s4, v0
	s_cbranch_vccnz .LBB0_2307
	v_ashrrev_i32_e32 v3, 31, v0
	v_lshrrev_b32_e32 v3, 26, v3
	v_lshlrev_b32_e32 v1, 4, v0
	v_add_u32_e32 v3, v0, v3
	v_bfe_i32 v0, v0, 27, 1
	v_lshrrev_b32_e32 v0, 22, v0
	v_add_u32_e32 v0, v1, v0
	v_and_b32_e32 v0, 0xfffffc00, v0
	v_sub_u32_e32 v0, v1, v0
	v_lshrrev_b32_e32 v4, 4, v0
	v_bitop3_b32 v0, v4, v0, 32 bitop3:0x6c
	v_ashrrev_i32_e32 v5, 31, v0
	v_ashrrev_i32_e32 v3, 6, v3
	v_lshrrev_b32_e32 v5, 26, v5
	v_lshlrev_b32_e32 v4, 3, v3
	v_add_u32_e32 v5, v0, v5
	v_and_b32_e32 v4, -16, v4
	v_ashrrev_i32_e32 v6, 6, v5
	v_add_u32_e32 v160, v6, v4
	v_and_b32_e32 v4, 0xc0, v5
	v_sub_u32_e32 v0, v0, v4
	v_mov_b32_e32 v4, 1
	v_lshlrev_b32_e32 v3, 5, v3
	v_ashrrev_i16_sdwa v0, v4, sext(v0) dst_sel:DWORD dst_unused:UNUSED_PAD src0_sel:DWORD src1_sel:BYTE_0
	v_and_b32_e32 v3, 32, v3
	v_bfe_i32 v0, v0, 0, 16
	v_add_lshl_u32 v161, v3, v0, 1
	v_add_u32_e32 v0, 0x2000, v1
	v_ashrrev_i32_e32 v1, 31, v0
	v_lshrrev_b32_e32 v1, 22, v1
	v_add_u32_e32 v1, v0, v1
	s_ashr_i32 s5, s2, 31
	v_ashrrev_i32_e32 v1, 10, v1
	s_lshr_b32 s5, s5, 29
	v_mul_i32_i24_e32 v3, 0x400, v1
	s_add_i32 s5, s2, s5
	v_sub_u32_e32 v0, v0, v3
	s_ashr_i32 s19, s5, 3
	s_and_b32 s5, s5, -8
	v_lshrrev_b32_e32 v3, 4, v0
	s_sub_i32 s2, s2, s5
	s_lshl_b32 s5, s68, 10
	v_bitop3_b32 v0, v3, v0, 32 bitop3:0x6c
	s_ashr_i32 s18, s4, 6
	s_add_i32 s5, s5, 0
	s_ashr_i32 s3, s4, 8
	v_ashrrev_i32_e32 v5, 31, v0
	s_lshl_b32 s17, s18, 10
	s_add_i32 s20, s5, 0x20000
	s_or_b32 s22, s63, 1
	v_lshrrev_b32_e32 v5, 26, v5
	s_cmp_lt_i32 s2, 0
	v_lshlrev_b32_e32 v3, 3, v1
	v_add_u32_e32 v5, v0, v5
	s_cselect_b32 s21, s22, s63
	v_and_b32_e32 v3, -16, v3
	v_ashrrev_i32_e32 v7, 6, v5
	s_mul_i32 s2, s21, s2
	v_add_u32_e32 v162, v7, v3
	v_and_b32_e32 v3, 0xc0, v5
	s_add_i32 s19, s2, s19
	v_sub_u32_e32 v0, v0, v3
	s_ashr_i32 s2, s19, 31
	v_lshlrev_b32_e32 v1, 5, v1
	v_ashrrev_i16_sdwa v0, v4, sext(v0) dst_sel:DWORD dst_unused:UNUSED_PAD src0_sel:DWORD src1_sel:BYTE_0
	s_lshr_b32 s2, s2, 28
	v_and_b32_e32 v1, 32, v1
	v_bfe_i32 v0, v0, 0, 16
	s_add_i32 s2, s19, s2
	v_add_lshl_u32 v163, v1, v0, 1
	v_and_b32_e32 v0, 3, v7
	s_mov_b32 s5, 0x1ffffe0
	v_lshrrev_b32_e32 v1, 2, v162
	v_lshlrev_b32_e32 v3, 1, v162
	s_ashr_i32 s2, s2, 4
	v_and_or_b32 v0, v162, s5, v0
	v_and_b32_e32 v1, 4, v1
	v_and_b32_e32 v3, 24, v3
	s_lshl_b32 s2, s2, 2
	s_add_i32 s23, 0, 0x26c00
	v_or3_b32 v0, v0, v1, v3
	s_add_i32 s2, s23, s2
	v_lshl_add_u32 v144, v0, 7, v163
	v_mov_b32_e32 v0, s2
	ds_read_b32 v88, v0
	v_and_b32_e32 v0, 3, v6
	v_and_or_b32 v3, v160, s5, v0
	v_lshrrev_b32_e32 v0, 2, v160
	v_and_b32_e32 v4, 4, v0
	s_waitcnt lgkmcnt(0)
	v_lshlrev_b32_e32 v0, 2, v88
	v_add_u32_e32 v0, s23, v0
	ds_read2st64_b32 v[0:1], v0 offset0:4 offset1:5
	v_lshlrev_b32_e32 v5, 1, v160
	v_and_b32_e32 v5, 24, v5
	v_or3_b32 v3, v3, v4, v5
	v_lshl_add_u32 v146, v3, 7, v161
	s_waitcnt lgkmcnt(0)
	v_readfirstlane_b32 s2, v1
	s_addk_i32 s2, 0xff
	s_ashr_i32 s2, s2, 8
	s_abs_i32 s21, s2
	v_cvt_f32_u32_e32 v1, s21
	v_readfirstlane_b32 s5, v0
	s_ashr_i32 s5, s5, 8
	s_sub_i32 s28, 0, s21
	v_rcp_iflag_f32_e32 v0, v1
	s_lshl_b32 s24, s5, 4
	s_sub_i32 s19, s19, s24
	s_abs_i32 s25, s19
	v_mul_f32_e32 v0, 0x4f7ffffe, v0
	v_cvt_u32_f32_e32 v0, v0
	s_xor_b32 s24, s19, s2
	s_ashr_i32 s24, s24, 31
	v_lshl_add_u32 v3, v162, 2, s20
	v_readfirstlane_b32 s29, v0
	s_mul_i32 s28, s28, s29
	s_mul_hi_u32 s28, s29, s28
	s_add_i32 s29, s29, s28
	s_mul_hi_u32 s28, s25, s29
	s_mul_i32 s29, s28, s21
	s_sub_i32 s25, s25, s29
	s_add_i32 s29, s28, 1
	s_sub_i32 s30, s25, s21
	s_cmp_ge_u32 s25, s21
	s_cselect_b32 s28, s29, s28
	s_cselect_b32 s25, s30, s25
	s_add_i32 s29, s28, 1
	s_cmp_ge_u32 s25, s21
	v_lshl_add_u32 v0, v160, 2, s20
	s_cselect_b32 s20, s29, s28
	ds_read2st64_b32 v[0:1], v0 offset1:2
	s_xor_b32 s20, s20, s24
	s_sub_i32 s56, s20, s24
	s_ashr_i32 s57, s56, 31
	ds_read2st64_b32 v[4:5], v3 offset1:2
	s_lshl_b64 s[20:21], s[56:57], 20
	v_ashrrev_i32_e32 v89, 31, v88
	s_add_u32 s20, s64, s20
	s_waitcnt lgkmcnt(1)
	v_lshl_add_u32 v148, v0, 12, v161
	v_lshl_add_u32 v92, v1, 12, v161
	s_addc_u32 s21, s65, s21
	v_lshlrev_b64 v[0:1], 24, v[88:89]
	v_lshl_add_u64 v[0:1], s[20:21], 0, v[0:1]
	s_add_i32 s24, s17, 0
	s_add_i32 m0, s24, 0x10000
	v_readfirstlane_b32 s20, v0
	v_readfirstlane_b32 s21, v1
	s_mov_b64 s[28:29], 0x4000
	s_waitcnt lgkmcnt(0)
	v_lshl_add_u32 v94, v4, 12, v163
	v_lshl_add_u32 v90, v5, 12, v163
	v_lshl_add_u64 v[4:5], v[0:1], 0, s[28:29]
	s_add_i32 s25, s24, 0x2000
	global_load_lds_dwordx4 v146, s[20:21]
	s_add_i32 m0, s24, 0x12000
	s_add_i32 s57, s24, 0x4000
	global_load_lds_dwordx4 v144, s[20:21]
	s_add_i32 m0, s24, 0x14000
	v_readfirstlane_b32 s20, v4
	v_readfirstlane_b32 s21, v5
	s_add_i32 s67, s24, 0x6000
	v_mov_b32_e32 v149, 0
	s_mov_b32 s69, 0
	v_mov_b32_e32 v147, v149
	v_mov_b32_e32 v145, v149
	global_load_lds_dwordx4 v146, s[20:21]
	s_add_i32 m0, s24, 0x16000
	s_cmp_eq_u32 s3, 1
	global_load_lds_dwordx4 v144, s[20:21]
	s_mov_b32 m0, s24
	s_cselect_b64 s[30:31], -1, 0
	global_load_lds_dwordx4 v148, s[14:15]
	s_mov_b32 m0, s25
	s_cmp_lg_u32 s3, 1
	global_load_lds_dwordx4 v94, s[14:15]
	s_mov_b32 m0, s57
	v_mov_b32_e32 v95, v149
	global_load_lds_dwordx4 v92, s[14:15]
	s_mov_b32 m0, s67
	s_nop 0
	global_load_lds_dwordx4 v90, s[14:15]
	s_setprio 1
	s_cbranch_scc1 .LBB0_2291
	s_setprio 0
	s_barrier

; #define PG8_WAIT_V(n) asm volatile("s_waitcnt vmcnt(" #n ")" ::: "memory")
; #define PG8_BAR __builtin_amdgcn_s_barrier()
; template <class Epi, class Sched, bool ALIGN_EPI = false, bool SP2 = false>
; __device__ __forceinline__ void gemm_phase(PG8_LAS unsigned char* lds, const Gemm g, const Sched& S, const Epi& E, const int tid_in) {
;     const int tid = tid_in, wid = __builtin_amdgcn_readfirstlane(tid >> 6), lane = tid & 63, wr = wid >> 2, wc = wid & 3, fr = lane & 15, fq = lane >> 4;
;     const int K = g.K, nt = K / BK, LDB = g.btiled ? 64 : K;
;     unsigned voffA[2], voffB[2]; unsigned vc[2][2] = {{0u, 0u}, {0u, 0u}}, vn[2][2] = {{0u, 0u}, {0u, 0u}}; int gR[2], gC[2];
; #pragma unroll
;     for (int i = 0; i < 2; ++i) { int R, C; stage_rc(tid * 16 + i * 8192, R, C); const int Rb = Epi::PERM ? ((R & ~31) + perm32(R & 31)) : R;
;         voffA[i] = (unsigned)(R * K + C) * 2u; voffB[i] = (unsigned)(Rb * LDB + C) * 2u; gR[i] = R; gC[i] = C * 2; }
;     const size_t kstep = (size_t)(BK * 2);
;     const size_t hstep = (size_t)HALF * K * 2;
;     const size_t tstep = 2 * hstep; const size_t kstepB = g.btiled ? (size_t)32768 : kstep, hstepB = g.btiled ? (size_t)16384 : hstep;
;     const unsigned ldsw = (unsigned)wid * 1024u;
;     const int aoff = lds_byte(wr * 64 + fr, fq * 8), boff = lds_byte(wc * 32 + fr, fq * 8);
;     ...
;     Unit cur, nxt; int ui = 0;
;     if (!S.next(0, cur)) return;
;     f32x4 acc[2][2][4][2];
; #pragma unroll
;     for (int a = 0; a < 2; ++a)
; #pragma unroll
;         for (int b = 0; b < 2; ++b)
; #pragma unroll
;             for (int m = 0; m < 4; ++m)
; #pragma unroll
;                 for (int n = 0; n < 2; ++n) acc[a][b][m][n] = (f32x4){0.f, 0.f, 0.f, 0.f};
;     bf16x8 At[4][2], B0[2][2], B1[2][2];
;     const char* cA = (const char*)g.A + (Sched::GATHER ? (size_t)0 : (size_t)cur.pm * tstep); if constexpr (Sched::GATHER) PG8_GFILL(vc, 0); const char* cB = (const char*)g.Bt + (size_t)cur.pn * tstep + (size_t)cur.e * g.estride;
;     S.a_ready(cur);
;     if constexpr (SP2) {
;         PG8_STAGE(PG8_SB(0, 0), cB, voffB); PG8_STAGE(PG8_SB(0, 1), cB + hstepB, voffB); PG8_STAGE_A(PG8_SA(0, 0), cA, 0, false); PG8_STAGE_A(PG8_SA(0, 1), cA, 1, false);
;         if (wr == 1) PG8_BAR;
;         PG8_WAIT_V(2); PG8_BAR;
.LBB0_3485:
	s_add_i32 s4, 0, 0x26e80
	s_waitcnt vmcnt(0)
	v_mov_b32_e32 v0, s4
	ds_read_b32 v0, v0
	s_waitcnt lgkmcnt(0)
	v_mbcnt_lo_u32_b32 v6, -1, 0
	v_mbcnt_hi_u32_b32 v6, -1, v6
	v_lshlrev_b32_e32 v144, 3, v0
	v_readfirstlane_b32 s17, v0
	v_add_u32_e32 v0, s33, v6
	v_cmp_ge_i32_e32 vcc, s81, v144
	v_readfirstlane_b32 s4, v0
	s_cbranch_vccnz .LBB0_3502
	v_lshlrev_b32_e32 v1, 4, v0
	v_add_u32_e32 v2, 0x2000, v1
	v_ashrrev_i32_e32 v3, 31, v2
	v_lshrrev_b32_e32 v3, 22, v3
	v_add_u32_e32 v3, v2, v3
	v_ashrrev_i32_e32 v7, 10, v3
	v_mul_i32_i24_e32 v3, 0x400, v7
	v_sub_u32_e32 v2, v2, v3
	v_lshrrev_b32_e32 v3, 4, v2
	v_bitop3_b32 v2, v3, v2, 32 bitop3:0x6c
	v_ashrrev_i32_e32 v3, 31, v2
	v_lshrrev_b32_e32 v3, 26, v3
	v_add_u32_e32 v3, v2, v3
	v_lshlrev_b32_e32 v4, 3, v7
	v_ashrrev_i32_e32 v8, 6, v3
	v_and_b32_e32 v4, -16, v4
	v_add_u32_e32 v4, v8, v4
	v_and_b32_e32 v5, 3, v8
	s_mov_b32 s12, 0x1ffffe0
	v_lshrrev_b32_e32 v9, 2, v4
	v_lshlrev_b32_e32 v10, 1, v4
	v_and_b32_e32 v3, 0xc0, v3
	v_and_or_b32 v5, v4, s12, v5
	v_and_b32_e32 v9, 4, v9
	v_and_b32_e32 v10, 24, v10
	v_sub_u32_e32 v2, v2, v3
	v_mov_b32_e32 v3, 1
	v_or3_b32 v5, v5, v9, v10
	v_lshlrev_b32_e32 v9, 5, v7
	v_ashrrev_i16_sdwa v2, v3, sext(v2) dst_sel:DWORD dst_unused:UNUSED_PAD src0_sel:DWORD src1_sel:BYTE_0
	v_and_b32_e32 v10, 32, v9
	v_bfe_i32 v9, v2, 0, 16
	v_add_lshl_u32 v2, v10, v9, 1
	v_lshl_add_u32 v146, v5, 7, v2
	v_lshl_add_u32 v148, v4, 12, v2
	v_bfe_i32 v2, v0, 27, 1
	v_lshrrev_b32_e32 v2, 22, v2
	v_add_u32_e32 v2, v1, v2
	s_add_u32 s22, s8, 0x64000000
	v_and_b32_e32 v2, 0xfffffc00, v2
	s_addc_u32 s23, s9, 0
	v_sub_u32_e32 v1, v1, v2
	s_add_u32 s24, s8, 0x26000000
	v_lshrrev_b32_e32 v2, 4, v1
	v_ashrrev_i32_e32 v4, 31, v0
	s_addc_u32 s25, s9, 0
	s_ashr_i32 s61, s81, 31
	v_bitop3_b32 v1, v2, v1, 32 bitop3:0x6c
	v_lshrrev_b32_e32 v4, 26, v4
	s_lshr_b32 s6, s61, 29
	v_ashrrev_i32_e32 v2, 31, v1
	v_add_u32_e32 v0, v0, v4
	s_add_i32 s6, s81, s6
	v_lshrrev_b32_e32 v2, 26, v2
	v_ashrrev_i32_e32 v11, 6, v0
	s_ashr_i32 s5, s4, 6
	s_ashr_i32 s7, s6, 3
	s_and_b32 s6, s6, -8
	v_add_u32_e32 v2, v1, v2
	v_lshlrev_b32_e32 v0, 3, v11
	s_ashr_i32 s20, s4, 8
	s_lshl_b32 s60, s5, 10
	s_sub_i32 s6, s81, s6
	s_add_i32 s62, s17, 1
	v_ashrrev_i32_e32 v10, 6, v2
	v_and_b32_e32 v0, -16, v0
	s_cmp_lt_i32 s6, 0
	v_add_u32_e32 v4, v10, v0
	v_and_b32_e32 v0, 3, v10
	v_and_or_b32 v0, v4, s12, v0
	s_cselect_b32 s12, s62, s17
	s_mul_i32 s6, s12, s6
	s_add_i32 s6, s6, s7
	s_ashr_i32 s7, s6, 31
	s_lshr_b32 s7, s7, 29
	s_add_i32 s7, s6, s7
	s_ashr_i32 s7, s7, 3
	v_lshrrev_b32_e32 v5, 2, v4
	v_lshlrev_b32_e32 v12, 1, v4
	s_lshl_b32 s7, s7, 2
	s_add_i32 s63, 0, 0x26c00
	v_and_b32_e32 v5, 4, v5
	v_and_b32_e32 v12, 24, v12
	s_add_i32 s7, s63, s7
	v_or3_b32 v5, v0, v5, v12
	v_mov_b32_e32 v12, s7
	ds_read_b32 v128, v12
	v_lshlrev_b32_e32 v0, 5, v11
	v_and_b32_e32 v13, 32, v0
	v_and_b32_e32 v0, 0xc0, v2
	v_sub_u32_e32 v0, v1, v0
	v_ashrrev_i16_sdwa v2, v3, sext(v0) dst_sel:DWORD dst_unused:UNUSED_PAD src0_sel:DWORD src1_sel:BYTE_0
	s_waitcnt lgkmcnt(0)
	v_lshlrev_b32_e32 v0, 2, v128
	v_add_u32_e32 v0, s63, v0
	ds_read2st64_b32 v[0:1], v0 offset0:4 offset1:5
	v_ashrrev_i32_e32 v129, 31, v128
	v_bfe_i32 v12, v2, 0, 16
	v_add_lshl_u32 v2, v13, v12, 1
	v_lshl_add_u32 v150, v5, 7, v2
	s_waitcnt lgkmcnt(0)
	v_readfirstlane_b32 s7, v1
	s_addk_i32 s7, 0xff
	s_ashr_i32 s7, s7, 8
	s_abs_i32 s12, s7
	v_cvt_f32_u32_e32 v1, s12
	v_readfirstlane_b32 s13, v0
	s_ashr_i32 s13, s13, 8
	s_sub_i32 s18, 0, s12
	v_rcp_iflag_f32_e32 v0, v1
	s_lshl_b32 s14, s13, 3
	s_sub_i32 s6, s6, s14
	s_abs_i32 s15, s6
	v_mul_f32_e32 v0, 0x4f7ffffe, v0
	v_cvt_u32_f32_e32 v0, v0
	s_xor_b32 s14, s6, s7
	s_ashr_i32 s14, s14, 31
	v_lshl_add_u32 v152, v4, 12, v2
	v_readfirstlane_b32 s19, v0
	s_mul_i32 s18, s18, s19
	s_mul_hi_u32 s18, s19, s18
	s_add_i32 s19, s19, s18
	s_mul_hi_u32 s18, s15, s19
	s_mul_i32 s19, s18, s12
	s_sub_i32 s15, s15, s19
	s_add_i32 s19, s18, 1
	s_sub_i32 s21, s15, s12
	s_cmp_ge_u32 s15, s12
	s_cselect_b32 s18, s19, s18
	s_cselect_b32 s15, s21, s15
	s_add_i32 s19, s18, 1
	s_cmp_ge_u32 s15, s12
	s_cselect_b32 s12, s19, s18
	s_xor_b32 s12, s12, s14
	s_sub_i32 s54, s12, s14
	s_mul_i32 s7, s54, s7
	s_sub_i32 s6, s6, s7
	s_add_i32 s52, s6, s13
	s_ashr_i32 s53, s52, 31
	s_ashr_i32 s55, s54, 31
	s_lshl_b64 s[12:13], s[52:53], 20
	s_lshl_b64 s[6:7], s[54:55], 20
	s_add_u32 s6, s24, s6
	s_addc_u32 s7, s25, s7
	v_lshlrev_b64 v[0:1], 23, v[128:129]
	v_lshl_add_u64 v[0:1], s[6:7], 0, v[0:1]
	s_add_i32 s18, s60, 0
	s_add_i32 m0, s18, 0x10000
	v_readfirstlane_b32 s6, v0
	v_readfirstlane_b32 s7, v1
	s_load_dwordx2 s[10:11], s[10:11], 0xb0
	v_mov_b32_e32 v151, 0
	v_mov_b32_e32 v153, v151
	v_mov_b32_e32 v149, v151
	v_mov_b32_e32 v147, v151
	global_load_lds_dwordx4 v150, s[6:7]
	s_add_i32 m0, s18, 0x12000
	s_nop 0
	global_load_lds_dwordx4 v146, s[6:7]
	s_mov_b64 s[6:7], 0x4000
	v_lshl_add_u64 v[2:3], v[0:1], 0, s[6:7]
	s_add_i32 m0, s18, 0x14000
	v_readfirstlane_b32 s14, v2
	v_readfirstlane_b32 s15, v3
	s_nop 4
	global_load_lds_dwordx4 v150, s[14:15]
	s_add_i32 m0, s18, 0x16000
	s_add_u32 s56, s22, s12
	s_addc_u32 s57, s23, s13
	s_add_i32 s19, s18, 0x2000
	global_load_lds_dwordx4 v146, s[14:15]
	s_mov_b32 m0, s18
	s_add_u32 s12, s56, 0x80000
	global_load_lds_dwordx4 v152, s[56:57]
	s_mov_b32 m0, s19
	s_addc_u32 s13, s57, 0
	s_add_i32 s53, s18, 0x4000
	global_load_lds_dwordx4 v148, s[56:57]
	s_mov_b32 m0, s53
	s_add_i32 s55, s18, 0x6000
	global_load_lds_dwordx4 v152, s[12:13]
	s_mov_b32 m0, s55
	s_cmp_eq_u32 s20, 1
	global_load_lds_dwordx4 v148, s[12:13]
	v_lshl_add_u64 v[4:5], s[56:57], 0, v[152:153]
	v_lshl_add_u64 v[2:3], s[56:57], 0, v[148:149]
	s_cselect_b64 s[12:13], -1, 0
	s_cmp_lg_u32 s20, 1
	s_mov_b64 s[14:15], 0x80000
	s_setprio 1
	s_cbranch_scc1 .LBB0_3488
	s_setprio 0
	s_barrier
